# static s_setprio 1 for the younger wave half (waves 4-7) during the mLSTM output unit
# baseline (speedup 1.0000x reference)
; #define FRESH() const int tid = TID(), lane = tid & 63, wave = __builtin_amdgcn_readfirstlane(tid >> 6); (void)lane; (void)wave
; #define PH(k, ...) if (IN(k)) { _Pragma("unroll") for (int rep_ = 0; rep_ < ((DUP_PHASE) == (k) ? 2 : 1); ++rep_) { if (rep_) xcd_barrier(bar, TID()); __VA_ARGS__ } } SEAM(k);
; __device__ __forceinline__ void ml_out_unit(const Args& a, unsigned char* lds_g, int u, int tid) {
;     const int L = u & 7, h = (u >> 3) & 7, b = u >> 6;
;     const int rowbase = NCTX + b * SEQ + 256 * L;
;     const int lane = tid & 63, w = __builtin_amdgcn_readfirstlane(tid >> 6), fr = lane & 15, fq = lane >> 4;
;     bf16* CB = (bf16*)(lds_g + ML_CB);
; __global__ void __launch_bounds__(NTHR, 2) fwd_kernel(Args args) {
;     ...
;     PH(3, { FRESH();
;         for (int u = c; u < 256; u += G) ml_out_unit(args, lds, u, tid);
.Lp3_ml:
	s_cmpk_gt_i32 s83, 0xff
	v_mbcnt_lo_u32_b32 v4, -1, 0
	v_mbcnt_hi_u32_b32 v4, -1, v4
	s_nop 0
	s_nop 0
	s_nop 0
	v_readlane_b32 s0, v249, 1
	s_nop 1
	v_or_b32_e32 v113, s0, v4
	s_cbranch_scc1 .LBB0_667
	v_readfirstlane_b32 s0, v113
	s_cmpk_gt_u32 s0, 0xff
	s_cbranch_scc0 .Lmlp_skip
	s_setprio 1
